# grid_barrier_leaders_poll_top_counter_directly
# speedup vs baseline: 1.0256x; 1.0026x over previous
.LBB0_226:
	s_or_b64 exec, exec, s[4:5]
	s_waitcnt vmcnt(0)
	v_readfirstlane_b32 s2, v4
	v_cvt_f32_u32_e32 v4, v2
	v_sub_u32_e32 v5, 0, v2
	v_add_u32_e32 v3, s2, v3
	s_mov_b64 s[4:5], -1
	v_rcp_iflag_f32_e32 v4, v4
	s_nop 0
	v_mul_f32_e32 v4, 0x4f7ffffe, v4
	v_cvt_u32_f32_e32 v4, v4
	v_mul_lo_u32 v5, v5, v4
	v_mul_hi_u32 v5, v4, v5
	v_add_u32_e32 v4, v4, v5
	v_mul_hi_u32 v4, v3, v4
	v_mul_lo_u32 v5, v4, v2
	v_sub_u32_e32 v5, v3, v5
	v_cmp_ge_u32_e32 vcc, v5, v2
	v_add_u32_e32 v6, 1, v4
	s_nop 0
	v_cndmask_b32_e32 v4, v4, v6, vcc
	v_sub_u32_e32 v6, v5, v2
	v_cndmask_b32_e32 v5, v5, v6, vcc
	v_cmp_ge_u32_e32 vcc, v5, v2
	v_add_u32_e32 v5, 1, v4
	s_nop 0
	v_cndmask_b32_e32 v4, v4, v5, vcc
	v_add_u32_e32 v5, 1, v3
	v_mad_u64_u32 v[2:3], s[2:3], v2, v4, v[2:3]
	v_mov_b32_e32 v6, v2
	v_readlane_b32 s2, v254, 27
	v_readlane_b32 s3, v254, 28
	v_cmp_ne_u32_e32 vcc, v5, v2
	s_nop 0
	v_mov_b64_e32 v[2:3], s[2:3]
	s_and_saveexec_b64 s[2:3], vcc
	s_cbranch_execz .LBB0_238
	v_readlane_b32 s4, v253, 30
	v_readlane_b32 s5, v253, 31
	s_mov_b64 s[6:7], 0
	s_nop 3
	global_load_dword v2, v195, s[4:5] sc1
	s_waitcnt vmcnt(0)
	v_cmp_lt_u32_e32 vcc, v2, v6
	s_and_saveexec_b64 s[4:5], vcc
	s_cbranch_execz .LBB0_237
	s_mov_b32 s16, 1
	s_branch .LBB0_230

.LBB0_232:
	v_readlane_b32 s10, v253, 30
	v_readlane_b32 s11, v253, 31
	s_add_i32 s16, s16, 1
	s_mov_b64 s[12:13], -1
	s_nop 2
	global_load_dword v2, v195, s[10:11] sc1
	s_waitcnt vmcnt(0)
	v_cmp_ge_u32_e32 vcc, v2, v6
	s_orn2_b64 s[10:11], vcc, exec
	s_branch .LBB0_229

.LBB0_334:
	s_or_b64 exec, exec, s[6:7]
	s_waitcnt vmcnt(0)
	v_readfirstlane_b32 s4, v4
	v_cvt_f32_u32_e32 v4, v2
	v_sub_u32_e32 v5, 0, v2
	v_add_u32_e32 v3, s4, v3
	s_mov_b64 s[6:7], -1
	v_rcp_iflag_f32_e32 v4, v4
	s_nop 0
	v_mul_f32_e32 v4, 0x4f7ffffe, v4
	v_cvt_u32_f32_e32 v4, v4
	v_mul_lo_u32 v5, v5, v4
	v_mul_hi_u32 v5, v4, v5
	v_add_u32_e32 v4, v4, v5
	v_mul_hi_u32 v4, v3, v4
	v_mul_lo_u32 v5, v4, v2
	v_sub_u32_e32 v5, v3, v5
	v_cmp_ge_u32_e32 vcc, v5, v2
	v_add_u32_e32 v6, 1, v4
	s_nop 0
	v_cndmask_b32_e32 v4, v4, v6, vcc
	v_sub_u32_e32 v6, v5, v2
	v_cndmask_b32_e32 v5, v5, v6, vcc
	v_cmp_ge_u32_e32 vcc, v5, v2
	v_add_u32_e32 v5, 1, v4
	s_nop 0
	v_cndmask_b32_e32 v4, v4, v5, vcc
	v_add_u32_e32 v5, 1, v3
	v_mad_u64_u32 v[2:3], s[4:5], v2, v4, v[2:3]
	v_mov_b32_e32 v6, v2
	v_readlane_b32 s4, v254, 27
	v_readlane_b32 s5, v254, 28
	v_cmp_ne_u32_e32 vcc, v5, v2
	s_nop 0
	v_mov_b64_e32 v[2:3], s[4:5]
	s_and_saveexec_b64 s[4:5], vcc
	s_cbranch_execz .LBB0_346
	v_readlane_b32 s6, v253, 30
	v_readlane_b32 s7, v253, 31
	s_mov_b64 s[8:9], 0
	s_nop 3
	global_load_dword v2, v195, s[6:7] sc1
	s_waitcnt vmcnt(0)
	v_cmp_lt_u32_e32 vcc, v2, v6
	s_and_saveexec_b64 s[6:7], vcc
	s_cbranch_execz .LBB0_345
	s_mov_b32 s18, 1
	s_branch .LBB0_338

.LBB0_340:
	v_readlane_b32 s12, v253, 30
	v_readlane_b32 s13, v253, 31
	s_add_i32 s18, s18, 1
	s_mov_b64 s[14:15], -1
	s_nop 2
	global_load_dword v2, v195, s[12:13] sc1
	s_waitcnt vmcnt(0)
	v_cmp_ge_u32_e32 vcc, v2, v6
	s_orn2_b64 s[12:13], vcc, exec
	s_branch .LBB0_337
